# gate/up GEMM: activation (ACT) stores marked non-temporal so they do not take L2 capacity from the tiles shared by concurrently running workgroups
# speedup vs baseline: 1.0085x; 1.0085x over previous
; #define GAS __attribute__((address_space(1)))
;     __device__ __forceinline__ void operator()(const f32x4 (&acc)[2][2][4][2], const Unit& u, const float (&rs)[2][4], int wr, int wc, int fr, int fq) const {
;         unsigned char* tp = O + (size_t)u.pm * (BM * DEXP) + (size_t)(u.pn * 2 + (wc >> 1)) * (BM * 64) + (wr * 64 + fr) * 64 + (wc & 1) * 32 + 8 * fq;
; #pragma unroll
;         for (int ai = 0; ai < 2; ++ai)
; #pragma unroll
;             for (int m = 0; m < 4; ++m) { unsigned char* rowp = tp + (ai * HALF + m * 16) * 64;
;                 float o[8];
; #pragma unroll
;                 for (int n = 0; n < 2; ++n)
; #pragma unroll
;                     for (int j = 0; j < 4; ++j) { const float g = acc[ai][0][m][n][j], uu = acc[ai][1][m][n][j];
;                         const float sg = g * __builtin_amdgcn_rcpf(1.0f + __builtin_amdgcn_exp2f(-g * LOG2E)); o[n * 4 + j] = __builtin_amdgcn_fmed3f(sg * uu, -448.0f, 448.0f); }
;                 int p0 = __builtin_amdgcn_cvt_pk_fp8_f32(o[0], o[1], 0, false); p0 = __builtin_amdgcn_cvt_pk_fp8_f32(o[2], o[3], p0, true);
;                 int p1 = __builtin_amdgcn_cvt_pk_fp8_f32(o[4], o[5], 0, false); p1 = __builtin_amdgcn_cvt_pk_fp8_f32(o[6], o[7], p1, true);
;                 u32x2_t wv; wv.x = (unsigned)p0; wv.y = (unsigned)p1;
;                 *(GAS u32x2_t*)rowp = wv; }
.LBB0_1600:
	s_mov_b32 s100, 0xbfb8aa3b
	s_mov_b32 s101, 0xbfb8aa3b
	s_ashr_i32 s41, s40, 31
	s_lshl_b64 s[62:63], s[40:41], 16
	s_add_u32 s41, s87, s62
	s_addc_u32 s64, s88, s63
	s_lshl_b32 s62, s9, 1
	s_or_b32 s62, s62, s92
	s_ashr_i32 s63, s62, 31
	s_lshl_b64 s[62:63], s[62:63], 14
	s_add_u32 s62, s41, s62
	s_addc_u32 s63, s64, s63
	v_lshl_add_u64 v[4:5], s[62:63], 0, v[206:207]
	v_lshl_add_u64 v[4:5], v[4:5], 0, s[22:23]
	v_lshl_add_u64 v[4:5], v[4:5], 0, v[204:205]
	s_movk_i32 s41, 0x2000
	v_pk_mul_f32 v[230:231], v[192:193], s[100:101] op_sel_hi:[1,0]
	v_pk_mul_f32 v[234:235], v[194:195], s[100:101] op_sel_hi:[1,0]
	v_pk_mul_f32 v[236:237], v[188:189], s[100:101] op_sel_hi:[1,0]
	v_pk_mul_f32 v[248:249], v[190:191], s[100:101] op_sel_hi:[1,0]
	v_exp_f32_e32 v230, v230
	v_exp_f32_e32 v231, v231
	v_exp_f32_e32 v234, v234
	v_exp_f32_e32 v235, v235
	v_exp_f32_e32 v236, v236
	v_exp_f32_e32 v237, v237
	v_exp_f32_e32 v248, v248
	v_exp_f32_e32 v249, v249
	v_pk_add_f32 v[230:231], v[230:231], 1.0 op_sel_hi:[1,0]
	v_pk_add_f32 v[234:235], v[234:235], 1.0 op_sel_hi:[1,0]
	v_pk_add_f32 v[236:237], v[236:237], 1.0 op_sel_hi:[1,0]
	v_pk_add_f32 v[248:249], v[248:249], 1.0 op_sel_hi:[1,0]
	v_rcp_f32_e32 v230, v230
	v_rcp_f32_e32 v231, v231
	v_rcp_f32_e32 v234, v234
	v_rcp_f32_e32 v235, v235
	v_rcp_f32_e32 v236, v236
	v_rcp_f32_e32 v237, v237
	v_rcp_f32_e32 v248, v248
	v_rcp_f32_e32 v249, v249
	v_pk_mul_f32 v[230:231], v[192:193], v[230:231]
	v_pk_mul_f32 v[234:235], v[194:195], v[234:235]
	v_pk_mul_f32 v[236:237], v[188:189], v[236:237]
	v_pk_mul_f32 v[248:249], v[190:191], v[248:249]
	v_pk_mul_f32 v[230:231], v[160:161], v[230:231]
	v_pk_mul_f32 v[234:235], v[162:163], v[234:235]
	v_pk_mul_f32 v[236:237], v[156:157], v[236:237]
	v_pk_mul_f32 v[248:249], v[158:159], v[248:249]
	v_med3_f32 v7, v230, s4, v233
	v_med3_f32 v8, v231, s4, v233
	v_med3_f32 v9, v234, s4, v233
	v_med3_f32 v10, v235, s4, v233
	v_med3_f32 v11, v236, s4, v233
	v_med3_f32 v12, v237, s4, v233
	v_med3_f32 v13, v248, s4, v233
	v_med3_f32 v14, v249, s4, v233
	v_mov_b32_e32 v6, v3
	v_cvt_pk_fp8_f32 v6, v7, v8
	v_mov_b32_e32 v7, v3
	v_cvt_pk_fp8_f32 v7, v11, v12
	v_cvt_pk_fp8_f32 v6, v9, v10 op_sel:[0,0,1]
	v_cvt_pk_fp8_f32 v7, v13, v14 op_sel:[0,0,1]
	global_store_dwordx2 v[4:5], v[6:7], off nt
	v_pk_mul_f32 v[230:231], v[184:185], s[100:101] op_sel_hi:[1,0]
	v_pk_mul_f32 v[234:235], v[186:187], s[100:101] op_sel_hi:[1,0]
	v_pk_mul_f32 v[236:237], v[180:181], s[100:101] op_sel_hi:[1,0]
	v_pk_mul_f32 v[248:249], v[182:183], s[100:101] op_sel_hi:[1,0]
	v_exp_f32_e32 v230, v230
	v_exp_f32_e32 v231, v231
	v_exp_f32_e32 v234, v234
	v_exp_f32_e32 v235, v235
	v_exp_f32_e32 v236, v236
	v_exp_f32_e32 v237, v237
	v_exp_f32_e32 v248, v248
	v_exp_f32_e32 v249, v249
	v_pk_add_f32 v[230:231], v[230:231], 1.0 op_sel_hi:[1,0]
	v_pk_add_f32 v[234:235], v[234:235], 1.0 op_sel_hi:[1,0]
	v_pk_add_f32 v[236:237], v[236:237], 1.0 op_sel_hi:[1,0]
	v_pk_add_f32 v[248:249], v[248:249], 1.0 op_sel_hi:[1,0]
	v_rcp_f32_e32 v230, v230
	v_rcp_f32_e32 v231, v231
	v_rcp_f32_e32 v234, v234
	v_rcp_f32_e32 v235, v235
	v_rcp_f32_e32 v236, v236
	v_rcp_f32_e32 v237, v237
	v_rcp_f32_e32 v248, v248
	v_rcp_f32_e32 v249, v249
	v_pk_mul_f32 v[230:231], v[184:185], v[230:231]
	v_pk_mul_f32 v[234:235], v[186:187], v[234:235]
	v_pk_mul_f32 v[236:237], v[180:181], v[236:237]
	v_pk_mul_f32 v[248:249], v[182:183], v[248:249]
	v_pk_mul_f32 v[230:231], v[152:153], v[230:231]
	v_pk_mul_f32 v[234:235], v[154:155], v[234:235]
	v_pk_mul_f32 v[236:237], v[148:149], v[236:237]
	v_pk_mul_f32 v[248:249], v[150:151], v[248:249]
	v_med3_f32 v7, v230, s4, v233
	v_med3_f32 v8, v231, s4, v233
	v_med3_f32 v9, v234, s4, v233
	v_med3_f32 v10, v235, s4, v233
	v_med3_f32 v11, v236, s4, v233
	v_med3_f32 v12, v237, s4, v233
	v_med3_f32 v13, v248, s4, v233
	v_med3_f32 v14, v249, s4, v233
	v_mov_b32_e32 v6, v3
	v_cvt_pk_fp8_f32 v6, v7, v8
	v_mov_b32_e32 v7, v3
	v_cvt_pk_fp8_f32 v7, v11, v12
	v_cvt_pk_fp8_f32 v6, v9, v10 op_sel:[0,0,1]
	v_cvt_pk_fp8_f32 v7, v13, v14 op_sel:[0,0,1]
	global_store_dwordx2 v[4:5], v[6:7], off offset:1024 nt
	v_pk_mul_f32 v[230:231], v[176:177], s[100:101] op_sel_hi:[1,0]
	v_pk_mul_f32 v[234:235], v[178:179], s[100:101] op_sel_hi:[1,0]
	v_pk_mul_f32 v[236:237], v[172:173], s[100:101] op_sel_hi:[1,0]
	v_pk_mul_f32 v[248:249], v[174:175], s[100:101] op_sel_hi:[1,0]
	v_exp_f32_e32 v230, v230
	v_exp_f32_e32 v231, v231
	v_exp_f32_e32 v234, v234
	v_exp_f32_e32 v235, v235
	v_exp_f32_e32 v236, v236
	v_exp_f32_e32 v237, v237
	v_exp_f32_e32 v248, v248
	v_exp_f32_e32 v249, v249
	v_pk_add_f32 v[230:231], v[230:231], 1.0 op_sel_hi:[1,0]
	v_pk_add_f32 v[234:235], v[234:235], 1.0 op_sel_hi:[1,0]
	v_pk_add_f32 v[236:237], v[236:237], 1.0 op_sel_hi:[1,0]
	v_pk_add_f32 v[248:249], v[248:249], 1.0 op_sel_hi:[1,0]
	v_rcp_f32_e32 v230, v230
	v_rcp_f32_e32 v231, v231
	v_rcp_f32_e32 v234, v234
	v_rcp_f32_e32 v235, v235
	v_rcp_f32_e32 v236, v236
	v_rcp_f32_e32 v237, v237
	v_rcp_f32_e32 v248, v248
	v_rcp_f32_e32 v249, v249
	v_pk_mul_f32 v[230:231], v[176:177], v[230:231]
	v_pk_mul_f32 v[234:235], v[178:179], v[234:235]
	v_pk_mul_f32 v[236:237], v[172:173], v[236:237]
	v_pk_mul_f32 v[248:249], v[174:175], v[248:249]
	v_pk_mul_f32 v[230:231], v[144:145], v[230:231]
	v_pk_mul_f32 v[234:235], v[146:147], v[234:235]
	v_pk_mul_f32 v[236:237], v[140:141], v[236:237]
	v_pk_mul_f32 v[248:249], v[142:143], v[248:249]
	v_med3_f32 v7, v230, s4, v233
	v_med3_f32 v8, v231, s4, v233
	v_med3_f32 v9, v234, s4, v233
	v_med3_f32 v10, v235, s4, v233
	v_med3_f32 v11, v236, s4, v233
	v_med3_f32 v12, v237, s4, v233
	v_med3_f32 v13, v248, s4, v233
	v_med3_f32 v14, v249, s4, v233
; #define GAS __attribute__((address_space(1)))
;     __device__ __forceinline__ void operator()(const f32x4 (&acc)[2][2][4][2], const Unit& u, const float (&rs)[2][4], int wr, int wc, int fr, int fq) const {
;         unsigned char* tp = O + (size_t)u.pm * (BM * DEXP) + (size_t)(u.pn * 2 + (wc >> 1)) * (BM * 64) + (wr * 64 + fr) * 64 + (wc & 1) * 32 + 8 * fq;
; #pragma unroll
;         for (int ai = 0; ai < 2; ++ai)
; #pragma unroll
;             for (int m = 0; m < 4; ++m) { unsigned char* rowp = tp + (ai * HALF + m * 16) * 64;
;                 float o[8];
; #pragma unroll
;                 for (int n = 0; n < 2; ++n)
; #pragma unroll
;                     for (int j = 0; j < 4; ++j) { const float g = acc[ai][0][m][n][j], uu = acc[ai][1][m][n][j];
;                         const float sg = g * __builtin_amdgcn_rcpf(1.0f + __builtin_amdgcn_exp2f(-g * LOG2E)); o[n * 4 + j] = __builtin_amdgcn_fmed3f(sg * uu, -448.0f, 448.0f); }
;                 int p0 = __builtin_amdgcn_cvt_pk_fp8_f32(o[0], o[1], 0, false); p0 = __builtin_amdgcn_cvt_pk_fp8_f32(o[2], o[3], p0, true);
;                 int p1 = __builtin_amdgcn_cvt_pk_fp8_f32(o[4], o[5], 0, false); p1 = __builtin_amdgcn_cvt_pk_fp8_f32(o[6], o[7], p1, true);
;                 u32x2_t wv; wv.x = (unsigned)p0; wv.y = (unsigned)p1;
;                 *(GAS u32x2_t*)rowp = wv; }
	v_mov_b32_e32 v6, v3
	v_cvt_pk_fp8_f32 v6, v7, v8
	v_mov_b32_e32 v7, v3
	v_cvt_pk_fp8_f32 v7, v11, v12
	v_cvt_pk_fp8_f32 v6, v9, v10 op_sel:[0,0,1]
	v_cvt_pk_fp8_f32 v7, v13, v14 op_sel:[0,0,1]
	global_store_dwordx2 v[4:5], v[6:7], off offset:2048 nt
	v_pk_mul_f32 v[230:231], v[168:169], s[100:101] op_sel_hi:[1,0]
	v_pk_mul_f32 v[234:235], v[170:171], s[100:101] op_sel_hi:[1,0]
	v_pk_mul_f32 v[236:237], v[164:165], s[100:101] op_sel_hi:[1,0]
	v_pk_mul_f32 v[248:249], v[166:167], s[100:101] op_sel_hi:[1,0]
	v_exp_f32_e32 v230, v230
	v_exp_f32_e32 v231, v231
	v_exp_f32_e32 v234, v234
	v_exp_f32_e32 v235, v235
	v_exp_f32_e32 v236, v236
	v_exp_f32_e32 v237, v237
	v_exp_f32_e32 v248, v248
	v_exp_f32_e32 v249, v249
	v_pk_add_f32 v[230:231], v[230:231], 1.0 op_sel_hi:[1,0]
	v_pk_add_f32 v[234:235], v[234:235], 1.0 op_sel_hi:[1,0]
	v_pk_add_f32 v[236:237], v[236:237], 1.0 op_sel_hi:[1,0]
	v_pk_add_f32 v[248:249], v[248:249], 1.0 op_sel_hi:[1,0]
	v_rcp_f32_e32 v230, v230
	v_rcp_f32_e32 v231, v231
	v_rcp_f32_e32 v234, v234
	v_rcp_f32_e32 v235, v235
	v_rcp_f32_e32 v236, v236
	v_rcp_f32_e32 v237, v237
	v_rcp_f32_e32 v248, v248
	v_rcp_f32_e32 v249, v249
	v_pk_mul_f32 v[230:231], v[168:169], v[230:231]
	v_pk_mul_f32 v[234:235], v[170:171], v[234:235]
	v_pk_mul_f32 v[236:237], v[164:165], v[236:237]
	v_pk_mul_f32 v[248:249], v[166:167], v[248:249]
	v_pk_mul_f32 v[230:231], v[136:137], v[230:231]
	v_pk_mul_f32 v[234:235], v[138:139], v[234:235]
	v_pk_mul_f32 v[236:237], v[132:133], v[236:237]
	v_pk_mul_f32 v[248:249], v[134:135], v[248:249]
	v_med3_f32 v7, v230, s4, v233
	v_med3_f32 v8, v231, s4, v233
	v_med3_f32 v9, v234, s4, v233
	v_med3_f32 v10, v235, s4, v233
	v_med3_f32 v11, v236, s4, v233
	v_med3_f32 v12, v237, s4, v233
	v_med3_f32 v13, v248, s4, v233
	v_med3_f32 v14, v249, s4, v233
	v_mov_b32_e32 v6, v3
	v_cvt_pk_fp8_f32 v6, v7, v8
	v_mov_b32_e32 v7, v3
	v_cvt_pk_fp8_f32 v7, v11, v12
	v_cvt_pk_fp8_f32 v6, v9, v10 op_sel:[0,0,1]
	v_cvt_pk_fp8_f32 v7, v13, v14 op_sel:[0,0,1]
	global_store_dwordx2 v[4:5], v[6:7], off offset:3072 nt
	v_add_co_u32_e32 v4, vcc, s41, v4
	s_nop 1
	v_addc_co_u32_e32 v5, vcc, 0, v5, vcc
	s_and_b64 vcc, exec, s[38:39]
	v_pk_mul_f32 v[230:231], v[128:129], s[100:101] op_sel_hi:[1,0]
	v_pk_mul_f32 v[234:235], v[130:131], s[100:101] op_sel_hi:[1,0]
	v_pk_mul_f32 v[236:237], v[124:125], s[100:101] op_sel_hi:[1,0]
	v_pk_mul_f32 v[248:249], v[126:127], s[100:101] op_sel_hi:[1,0]
	v_exp_f32_e32 v230, v230
	v_exp_f32_e32 v231, v231
	v_exp_f32_e32 v234, v234
	v_exp_f32_e32 v235, v235
	v_exp_f32_e32 v236, v236
	v_exp_f32_e32 v237, v237
	v_exp_f32_e32 v248, v248
	v_exp_f32_e32 v249, v249
	v_pk_add_f32 v[230:231], v[230:231], 1.0 op_sel_hi:[1,0]
	v_pk_add_f32 v[234:235], v[234:235], 1.0 op_sel_hi:[1,0]
	v_pk_add_f32 v[236:237], v[236:237], 1.0 op_sel_hi:[1,0]
	v_pk_add_f32 v[248:249], v[248:249], 1.0 op_sel_hi:[1,0]
	v_rcp_f32_e32 v230, v230
	v_rcp_f32_e32 v231, v231
	v_rcp_f32_e32 v234, v234
	v_rcp_f32_e32 v235, v235
	v_rcp_f32_e32 v236, v236
	v_rcp_f32_e32 v237, v237
	v_rcp_f32_e32 v248, v248
	v_rcp_f32_e32 v249, v249
	v_pk_mul_f32 v[230:231], v[128:129], v[230:231]
	v_pk_mul_f32 v[234:235], v[130:131], v[234:235]
	v_pk_mul_f32 v[236:237], v[124:125], v[236:237]
	v_pk_mul_f32 v[248:249], v[126:127], v[248:249]
	v_pk_mul_f32 v[230:231], v[96:97], v[230:231]
	v_pk_mul_f32 v[234:235], v[98:99], v[234:235]
	v_pk_mul_f32 v[236:237], v[92:93], v[236:237]
	v_pk_mul_f32 v[248:249], v[94:95], v[248:249]
	v_med3_f32 v7, v230, s4, v233
	v_med3_f32 v8, v231, s4, v233
	v_med3_f32 v9, v234, s4, v233
	v_med3_f32 v10, v235, s4, v233
	v_med3_f32 v11, v236, s4, v233
	v_med3_f32 v12, v237, s4, v233
	v_med3_f32 v13, v248, s4, v233
	v_med3_f32 v14, v249, s4, v233
	v_mov_b32_e32 v6, v3
	v_cvt_pk_fp8_f32 v6, v7, v8
	v_mov_b32_e32 v7, v3
	v_cvt_pk_fp8_f32 v7, v11, v12
	v_cvt_pk_fp8_f32 v6, v9, v10 op_sel:[0,0,1]
	v_cvt_pk_fp8_f32 v7, v13, v14 op_sel:[0,0,1]
	global_store_dwordx2 v[4:5], v[6:7], off nt
	v_pk_mul_f32 v[230:231], v[120:121], s[100:101] op_sel_hi:[1,0]
	v_pk_mul_f32 v[234:235], v[122:123], s[100:101] op_sel_hi:[1,0]
	v_pk_mul_f32 v[236:237], v[116:117], s[100:101] op_sel_hi:[1,0]
	v_pk_mul_f32 v[248:249], v[118:119], s[100:101] op_sel_hi:[1,0]
	v_exp_f32_e32 v230, v230
	v_exp_f32_e32 v231, v231
	v_exp_f32_e32 v234, v234
	v_exp_f32_e32 v235, v235
	v_exp_f32_e32 v236, v236
	v_exp_f32_e32 v237, v237
	v_exp_f32_e32 v248, v248
	v_exp_f32_e32 v249, v249
	v_pk_add_f32 v[230:231], v[230:231], 1.0 op_sel_hi:[1,0]
	v_pk_add_f32 v[234:235], v[234:235], 1.0 op_sel_hi:[1,0]
	v_pk_add_f32 v[236:237], v[236:237], 1.0 op_sel_hi:[1,0]
	v_pk_add_f32 v[248:249], v[248:249], 1.0 op_sel_hi:[1,0]
	v_rcp_f32_e32 v230, v230
	v_rcp_f32_e32 v231, v231
	v_rcp_f32_e32 v234, v234
; #define GAS __attribute__((address_space(1)))
;     __device__ __forceinline__ void operator()(const f32x4 (&acc)[2][2][4][2], const Unit& u, const float (&rs)[2][4], int wr, int wc, int fr, int fq) const {
;         unsigned char* tp = O + (size_t)u.pm * (BM * DEXP) + (size_t)(u.pn * 2 + (wc >> 1)) * (BM * 64) + (wr * 64 + fr) * 64 + (wc & 1) * 32 + 8 * fq;
; #pragma unroll
;         for (int ai = 0; ai < 2; ++ai)
; #pragma unroll
;             for (int m = 0; m < 4; ++m) { unsigned char* rowp = tp + (ai * HALF + m * 16) * 64;
;                 float o[8];
; #pragma unroll
;                 for (int n = 0; n < 2; ++n)
; #pragma unroll
;                     for (int j = 0; j < 4; ++j) { const float g = acc[ai][0][m][n][j], uu = acc[ai][1][m][n][j];
;                         const float sg = g * __builtin_amdgcn_rcpf(1.0f + __builtin_amdgcn_exp2f(-g * LOG2E)); o[n * 4 + j] = __builtin_amdgcn_fmed3f(sg * uu, -448.0f, 448.0f); }
;                 int p0 = __builtin_amdgcn_cvt_pk_fp8_f32(o[0], o[1], 0, false); p0 = __builtin_amdgcn_cvt_pk_fp8_f32(o[2], o[3], p0, true);
;                 int p1 = __builtin_amdgcn_cvt_pk_fp8_f32(o[4], o[5], 0, false); p1 = __builtin_amdgcn_cvt_pk_fp8_f32(o[6], o[7], p1, true);
;                 u32x2_t wv; wv.x = (unsigned)p0; wv.y = (unsigned)p1;
;                 *(GAS u32x2_t*)rowp = wv; }
	v_rcp_f32_e32 v235, v235
	v_rcp_f32_e32 v236, v236
	v_rcp_f32_e32 v237, v237
	v_rcp_f32_e32 v248, v248
	v_rcp_f32_e32 v249, v249
	v_pk_mul_f32 v[230:231], v[120:121], v[230:231]
	v_pk_mul_f32 v[234:235], v[122:123], v[234:235]
	v_pk_mul_f32 v[236:237], v[116:117], v[236:237]
	v_pk_mul_f32 v[248:249], v[118:119], v[248:249]
	v_pk_mul_f32 v[230:231], v[88:89], v[230:231]
	v_pk_mul_f32 v[234:235], v[90:91], v[234:235]
	v_pk_mul_f32 v[236:237], v[84:85], v[236:237]
	v_pk_mul_f32 v[248:249], v[86:87], v[248:249]
	v_med3_f32 v7, v230, s4, v233
	v_med3_f32 v8, v231, s4, v233
	v_med3_f32 v9, v234, s4, v233
	v_med3_f32 v10, v235, s4, v233
	v_med3_f32 v11, v236, s4, v233
	v_med3_f32 v12, v237, s4, v233
	v_med3_f32 v13, v248, s4, v233
	v_med3_f32 v14, v249, s4, v233
	v_mov_b32_e32 v6, v3
	v_cvt_pk_fp8_f32 v6, v7, v8
	v_mov_b32_e32 v7, v3
	v_cvt_pk_fp8_f32 v7, v11, v12
	v_cvt_pk_fp8_f32 v6, v9, v10 op_sel:[0,0,1]
	v_cvt_pk_fp8_f32 v7, v13, v14 op_sel:[0,0,1]
	global_store_dwordx2 v[4:5], v[6:7], off offset:1024 nt
	v_pk_mul_f32 v[230:231], v[112:113], s[100:101] op_sel_hi:[1,0]
	v_pk_mul_f32 v[234:235], v[114:115], s[100:101] op_sel_hi:[1,0]
	v_pk_mul_f32 v[236:237], v[108:109], s[100:101] op_sel_hi:[1,0]
	v_pk_mul_f32 v[248:249], v[110:111], s[100:101] op_sel_hi:[1,0]
	v_exp_f32_e32 v230, v230
	v_exp_f32_e32 v231, v231
	v_exp_f32_e32 v234, v234
	v_exp_f32_e32 v235, v235
	v_exp_f32_e32 v236, v236
	v_exp_f32_e32 v237, v237
	v_exp_f32_e32 v248, v248
	v_exp_f32_e32 v249, v249
	v_pk_add_f32 v[230:231], v[230:231], 1.0 op_sel_hi:[1,0]
	v_pk_add_f32 v[234:235], v[234:235], 1.0 op_sel_hi:[1,0]
	v_pk_add_f32 v[236:237], v[236:237], 1.0 op_sel_hi:[1,0]
	v_pk_add_f32 v[248:249], v[248:249], 1.0 op_sel_hi:[1,0]
	v_rcp_f32_e32 v230, v230
	v_rcp_f32_e32 v231, v231
	v_rcp_f32_e32 v234, v234
	v_rcp_f32_e32 v235, v235
	v_rcp_f32_e32 v236, v236
	v_rcp_f32_e32 v237, v237
	v_rcp_f32_e32 v248, v248
	v_rcp_f32_e32 v249, v249
	v_pk_mul_f32 v[230:231], v[112:113], v[230:231]
	v_pk_mul_f32 v[234:235], v[114:115], v[234:235]
	v_pk_mul_f32 v[236:237], v[108:109], v[236:237]
	v_pk_mul_f32 v[248:249], v[110:111], v[248:249]
	v_pk_mul_f32 v[230:231], v[80:81], v[230:231]
	v_pk_mul_f32 v[234:235], v[82:83], v[234:235]
	v_pk_mul_f32 v[236:237], v[76:77], v[236:237]
	v_pk_mul_f32 v[248:249], v[78:79], v[248:249]
	v_med3_f32 v7, v230, s4, v233
	v_med3_f32 v8, v231, s4, v233
	v_med3_f32 v9, v234, s4, v233
	v_med3_f32 v10, v235, s4, v233
	v_med3_f32 v11, v236, s4, v233
	v_med3_f32 v12, v237, s4, v233
	v_med3_f32 v13, v248, s4, v233
	v_med3_f32 v14, v249, s4, v233
	v_mov_b32_e32 v6, v3
	v_cvt_pk_fp8_f32 v6, v7, v8
	v_mov_b32_e32 v7, v3
	v_cvt_pk_fp8_f32 v7, v11, v12
	v_cvt_pk_fp8_f32 v6, v9, v10 op_sel:[0,0,1]
	v_cvt_pk_fp8_f32 v7, v13, v14 op_sel:[0,0,1]
	global_store_dwordx2 v[4:5], v[6:7], off offset:2048 nt
	v_pk_mul_f32 v[230:231], v[104:105], s[100:101] op_sel_hi:[1,0]
	v_pk_mul_f32 v[234:235], v[106:107], s[100:101] op_sel_hi:[1,0]
	v_pk_mul_f32 v[236:237], v[100:101], s[100:101] op_sel_hi:[1,0]
	v_pk_mul_f32 v[248:249], v[102:103], s[100:101] op_sel_hi:[1,0]
	v_exp_f32_e32 v230, v230
	v_exp_f32_e32 v231, v231
	v_exp_f32_e32 v234, v234
	v_exp_f32_e32 v235, v235
	v_exp_f32_e32 v236, v236
	v_exp_f32_e32 v237, v237
	v_exp_f32_e32 v248, v248
	v_exp_f32_e32 v249, v249
	v_pk_add_f32 v[230:231], v[230:231], 1.0 op_sel_hi:[1,0]
	v_pk_add_f32 v[234:235], v[234:235], 1.0 op_sel_hi:[1,0]
	v_pk_add_f32 v[236:237], v[236:237], 1.0 op_sel_hi:[1,0]
	v_pk_add_f32 v[248:249], v[248:249], 1.0 op_sel_hi:[1,0]
	v_rcp_f32_e32 v230, v230
	v_rcp_f32_e32 v231, v231
	v_rcp_f32_e32 v234, v234
	v_rcp_f32_e32 v235, v235
	v_rcp_f32_e32 v236, v236
	v_rcp_f32_e32 v237, v237
	v_rcp_f32_e32 v248, v248
	v_rcp_f32_e32 v249, v249
	v_pk_mul_f32 v[230:231], v[104:105], v[230:231]
	v_pk_mul_f32 v[234:235], v[106:107], v[234:235]
	v_pk_mul_f32 v[236:237], v[100:101], v[236:237]
	v_pk_mul_f32 v[248:249], v[102:103], v[248:249]
	v_pk_mul_f32 v[230:231], v[72:73], v[230:231]
	v_pk_mul_f32 v[234:235], v[74:75], v[234:235]
	v_pk_mul_f32 v[236:237], v[68:69], v[236:237]
	v_pk_mul_f32 v[248:249], v[70:71], v[248:249]
	v_med3_f32 v7, v230, s4, v233
	v_med3_f32 v8, v231, s4, v233
	v_med3_f32 v9, v234, s4, v233
	v_med3_f32 v10, v235, s4, v233
	v_med3_f32 v11, v236, s4, v233
	v_med3_f32 v12, v237, s4, v233
	v_med3_f32 v13, v248, s4, v233
	v_med3_f32 v14, v249, s4, v233
	v_mov_b32_e32 v6, v3
	v_cvt_pk_fp8_f32 v6, v7, v8
	v_mov_b32_e32 v7, v3
	v_cvt_pk_fp8_f32 v7, v11, v12
	v_cvt_pk_fp8_f32 v6, v9, v10 op_sel:[0,0,1]
	v_cvt_pk_fp8_f32 v7, v13, v14 op_sel:[0,0,1]
	global_store_dwordx2 v[4:5], v[6:7], off offset:3072 nt
	s_cbranch_vccnz .LBB0_1566
	s_andn2_b64 vcc, exec, s[48:49]
	s_cbranch_vccnz .LBB0_1565
	s_barrier
	s_branch .LBB0_1565
